# P10 output stores write-through (sc0 sc1)
# baseline (speedup 1.0000x reference)
.LBB0_1224:
	s_add_i32 s2, s6, 1
	v_mov_b32_e32 v50, s6
	s_waitcnt vmcnt(2)
	v_cvt_pk_f32_fp8_e32 v[134:135], v6
	v_cvt_pk_f32_fp8_sdwa v[136:137], v6 src0_sel:WORD_1
	v_mov_b32_e32 v6, s2
	v_cmp_lt_i32_e32 vcc, s2, v46
	v_and_or_b32 v49, s6, 63, v33
	s_waitcnt vmcnt(1)
	v_lshlrev_b32_e32 v118, 16, v12
	v_cndmask_b32_e32 v6, v50, v6, vcc
	v_and_b32_e32 v119, 0xffff0000, v12
	v_lshlrev_b32_e32 v120, 16, v13
	v_and_b32_e32 v121, 0xffff0000, v13
	v_mad_u64_u32 v[12:13], s[6:7], v6, s3, v[32:33]
	v_and_or_b32 v6, v6, 63, v33
	v_lshlrev_b32_e32 v6, 2, v6
	v_cvt_pk_f32_fp8_e32 v[66:67], v24
	v_cvt_pk_f32_fp8_sdwa v[68:69], v24 src0_sel:WORD_1
	v_cvt_pk_f32_fp8_e32 v[90:91], v26
	v_cvt_pk_f32_fp8_sdwa v[92:93], v26 src0_sel:WORD_1
	ds_bpermute_b32 v24, v6, v47
	ds_bpermute_b32 v26, v6, v48
	v_ashrrev_i32_e32 v13, 31, v12
	v_cvt_pk_f32_fp8_e32 v[78:79], v25
	v_cvt_pk_f32_fp8_sdwa v[80:81], v25 src0_sel:WORD_1
	v_cvt_pk_f32_fp8_e32 v[102:103], v27
	v_cvt_pk_f32_fp8_sdwa v[104:105], v27 src0_sel:WORD_1
	v_lshlrev_b64 v[12:13], 12, v[12:13]
	s_waitcnt lgkmcnt(1)
	v_ashrrev_i32_e32 v25, 31, v24
	s_waitcnt lgkmcnt(0)
	v_ashrrev_i32_e32 v27, 31, v26
	v_lshl_add_u64 v[50:51], v[40:41], 0, v[12:13]
	v_lshlrev_b64 v[24:25], 11, v[24:25]
	v_lshlrev_b64 v[26:27], 11, v[26:27]
	v_cvt_pk_f32_fp8_e32 v[62:63], v20
	v_cvt_pk_f32_fp8_sdwa v[64:65], v20 src0_sel:WORD_1
	v_lshlrev_b32_e32 v70, 16, v28
	v_and_b32_e32 v71, 0xffff0000, v28
	v_lshlrev_b32_e32 v72, 16, v29
	v_and_b32_e32 v73, 0xffff0000, v29
	v_cvt_pk_f32_fp8_e32 v[74:75], v21
	v_cvt_pk_f32_fp8_sdwa v[76:77], v21 src0_sel:WORD_1
	v_lshlrev_b32_e32 v82, 16, v30
	v_and_b32_e32 v83, 0xffff0000, v30
	v_lshlrev_b32_e32 v84, 16, v31
	v_and_b32_e32 v85, 0xffff0000, v31
	v_cvt_pk_f32_fp8_e32 v[86:87], v22
	v_cvt_pk_f32_fp8_sdwa v[88:89], v22 src0_sel:WORD_1
	v_lshlrev_b32_e32 v94, 16, v16
	v_and_b32_e32 v95, 0xffff0000, v16
	v_lshlrev_b32_e32 v96, 16, v17
	v_and_b32_e32 v97, 0xffff0000, v17
	v_cvt_pk_f32_fp8_e32 v[98:99], v23
	v_cvt_pk_f32_fp8_sdwa v[100:101], v23 src0_sel:WORD_1
	v_lshlrev_b32_e32 v106, 16, v18
	v_and_b32_e32 v107, 0xffff0000, v18
	v_lshlrev_b32_e32 v108, 16, v19
	v_and_b32_e32 v109, 0xffff0000, v19
	v_cvt_pk_f32_fp8_e32 v[114:115], v4
	v_cvt_pk_f32_fp8_sdwa v[116:117], v4 src0_sel:WORD_1
	v_cvt_pk_f32_fp8_e32 v[124:125], v5
	v_cvt_pk_f32_fp8_sdwa v[126:127], v5 src0_sel:WORD_1
	v_lshlrev_b32_e32 v4, 16, v14
	v_and_b32_e32 v5, 0xffff0000, v14
	v_lshlrev_b32_e32 v128, 16, v15
	v_and_b32_e32 v129, 0xffff0000, v15
	global_load_dwordx4 v[28:31], v[50:51], off
	global_load_dwordx4 v[16:19], v[50:51], off offset:16
	global_load_dwordx4 v[12:15], v[50:51], off offset:2048
	global_load_dwordx4 v[20:23], v[50:51], off offset:2064
	v_lshl_add_u64 v[58:59], v[38:39], 0, v[24:25]
	v_lshl_add_u64 v[50:51], v[38:39], 0, v[26:27]
	global_load_dwordx4 v[24:27], v[50:51], off
	s_nop 0
	global_load_dwordx4 v[50:53], v[50:51], off offset:1024
	s_nop 0
	global_load_dwordx4 v[54:57], v[58:59], off
	s_nop 0
	global_load_dwordx4 v[58:61], v[58:59], off offset:1024
	v_lshlrev_b32_e32 v49, 2, v49
	ds_bpermute_b32 v148, v49, v34
	ds_bpermute_b32 v150, v49, v35
	v_cvt_pk_f32_fp8_e32 v[110:111], v8
	v_cvt_pk_f32_fp8_sdwa v[112:113], v8 src0_sel:WORD_1
	v_cvt_pk_f32_fp8_e32 v[122:123], v9
	v_cvt_pk_f32_fp8_sdwa v[8:9], v9 src0_sel:WORD_1
	v_cvt_pk_f32_fp8_e32 v[130:131], v10
	v_cvt_pk_f32_fp8_sdwa v[132:133], v10 src0_sel:WORD_1
	v_cvt_pk_f32_fp8_e32 v[140:141], v11
	v_cvt_pk_f32_fp8_sdwa v[10:11], v11 src0_sel:WORD_1
	v_ashrrev_i32_e32 v45, 31, v44
	v_cvt_pk_f32_fp8_e32 v[142:143], v7
	v_cvt_pk_f32_fp8_sdwa v[144:145], v7 src0_sel:WORD_1
	v_lshlrev_b64 v[146:147], 13, v[44:45]
	s_waitcnt vmcnt(8)
	v_lshlrev_b32_e32 v138, 16, v0
	v_and_b32_e32 v139, 0xffff0000, v0
	v_lshlrev_b32_e32 v0, 16, v1
	v_and_b32_e32 v1, 0xffff0000, v1
	v_lshlrev_b32_e32 v6, 16, v2
	v_and_b32_e32 v7, 0xffff0000, v2
	v_lshlrev_b32_e32 v2, 16, v3
	v_and_b32_e32 v3, 0xffff0000, v3
	v_lshl_add_u64 v[146:147], s[4:5], 0, v[146:147]
	s_waitcnt lgkmcnt(1)
	v_pk_fma_f32 v[62:63], v[62:63], v[148:149], v[70:71] op_sel_hi:[1,0,1]
	v_pk_fma_f32 v[64:65], v[64:65], v[148:149], v[72:73] op_sel_hi:[1,0,1]
	v_pk_fma_f32 v[70:71], v[74:75], v[148:149], v[82:83] op_sel_hi:[1,0,1]
	v_pk_fma_f32 v[72:73], v[76:77], v[148:149], v[84:85] op_sel_hi:[1,0,1]
	v_pk_fma_f32 v[74:75], v[86:87], v[148:149], v[94:95] op_sel_hi:[1,0,1]
	v_pk_fma_f32 v[76:77], v[88:89], v[148:149], v[96:97] op_sel_hi:[1,0,1]
	v_mov_b32_e32 v43, v37
	v_lshl_add_u64 v[152:153], v[146:147], 0, v[36:37]
	v_pk_fma_f32 v[82:83], v[98:99], v[148:149], v[106:107] op_sel_hi:[1,0,1]
	v_pk_fma_f32 v[84:85], v[100:101], v[148:149], v[108:109] op_sel_hi:[1,0,1]
	v_pk_fma_f32 v[86:87], v[110:111], v[148:149], v[118:119] op_sel_hi:[1,0,1]
	v_pk_fma_f32 v[88:89], v[112:113], v[148:149], v[120:121] op_sel_hi:[1,0,1]
	v_pk_fma_f32 v[94:95], v[122:123], v[148:149], v[4:5] op_sel_hi:[1,0,1]
	v_pk_fma_f32 v[96:97], v[8:9], v[148:149], v[128:129] op_sel_hi:[1,0,1]
	v_pk_fma_f32 v[98:99], v[130:131], v[148:149], v[138:139] op_sel_hi:[1,0,1]
	v_pk_fma_f32 v[100:101], v[132:133], v[148:149], v[0:1] op_sel_hi:[1,0,1]
	v_pk_fma_f32 v[106:107], v[140:141], v[148:149], v[6:7] op_sel_hi:[1,0,1]
	v_pk_fma_f32 v[108:109], v[10:11], v[148:149], v[2:3] op_sel_hi:[1,0,1]
	s_waitcnt lgkmcnt(0)
	v_pk_fma_f32 v[0:1], v[66:67], v[150:151], v[62:63] op_sel_hi:[1,0,1]
	v_pk_fma_f32 v[2:3], v[68:69], v[150:151], v[64:65] op_sel_hi:[1,0,1]
	v_pk_fma_f32 v[4:5], v[78:79], v[150:151], v[70:71] op_sel_hi:[1,0,1]
	v_pk_fma_f32 v[6:7], v[80:81], v[150:151], v[72:73] op_sel_hi:[1,0,1]
	v_pk_fma_f32 v[8:9], v[90:91], v[150:151], v[74:75] op_sel_hi:[1,0,1]
	v_pk_fma_f32 v[10:11], v[92:93], v[150:151], v[76:77] op_sel_hi:[1,0,1]
	v_cmp_eq_u32_e32 vcc, s2, v46
	v_lshl_add_u64 v[146:147], v[146:147], 0, v[42:43]
	v_pk_fma_f32 v[62:63], v[102:103], v[150:151], v[82:83] op_sel_hi:[1,0,1]
	v_pk_fma_f32 v[64:65], v[104:105], v[150:151], v[84:85] op_sel_hi:[1,0,1]
	v_pk_fma_f32 v[66:67], v[114:115], v[150:151], v[86:87] op_sel_hi:[1,0,1]
	v_pk_fma_f32 v[68:69], v[116:117], v[150:151], v[88:89] op_sel_hi:[1,0,1]
	v_pk_fma_f32 v[70:71], v[124:125], v[150:151], v[94:95] op_sel_hi:[1,0,1]
	v_pk_fma_f32 v[72:73], v[126:127], v[150:151], v[96:97] op_sel_hi:[1,0,1]
	v_pk_fma_f32 v[74:75], v[134:135], v[150:151], v[98:99] op_sel_hi:[1,0,1]
	v_pk_fma_f32 v[76:77], v[136:137], v[150:151], v[100:101] op_sel_hi:[1,0,1]
	v_pk_fma_f32 v[78:79], v[142:143], v[150:151], v[106:107] op_sel_hi:[1,0,1]
	v_pk_fma_f32 v[80:81], v[144:145], v[150:151], v[108:109] op_sel_hi:[1,0,1]
	global_store_dwordx4 v[152:153], v[0:3], off sc0 sc1
	global_store_dwordx4 v[152:153], v[4:7], off offset:16 sc0 sc1
	global_store_dwordx4 v[152:153], v[8:11], off offset:32 sc0 sc1
	global_store_dwordx4 v[152:153], v[62:65], off offset:48 sc0 sc1
	global_store_dwordx4 v[146:147], v[66:69], off sc0 sc1
	global_store_dwordx4 v[146:147], v[70:73], off offset:16 sc0 sc1
	global_store_dwordx4 v[146:147], v[74:77], off offset:32 sc0 sc1
	global_store_dwordx4 v[146:147], v[78:81], off offset:48 sc0 sc1
	v_add_u32_e32 v44, s3, v44
	s_mov_b32 s6, s2
	s_or_b64 s[0:1], vcc, s[0:1]
	s_waitcnt vmcnt(12)
	v_mov_b32_e32 v0, v20
	v_mov_b32_e32 v1, v21
	v_mov_b32_e32 v2, v22
	v_mov_b32_e32 v3, v23
	s_waitcnt vmcnt(10)
	v_mov_b64_e32 v[4:5], v[50:51]
	s_waitcnt vmcnt(9)
	v_mov_b64_e32 v[20:21], v[54:55]
	s_waitcnt vmcnt(8)
	v_mov_b64_e32 v[8:9], v[58:59]
	v_mov_b64_e32 v[6:7], v[52:53]
	v_mov_b64_e32 v[22:23], v[56:57]
	v_mov_b64_e32 v[10:11], v[60:61]
	s_andn2_b64 exec, exec, s[0:1]
	s_cbranch_execnz .LBB0_1224
